# gate/up epilogue: store base address computed once (3 other stores = base+const), 16 redundant zero-init v_mov before cvt_pk_fp8 pairs removed
# speedup vs baseline: 1.0082x; 1.0082x over previous
.LBB0_252:
	s_nop 15
	s_nop 15
	v_ashrrev_i32_e32 v23, 31, v22
	s_ashr_i32 s67, s66, 31
	s_add_u32 s100, s50, s66
	s_addc_u32 s101, s51, s67
	s_add_u32 s100, s100, s52
	s_addc_u32 s101, s101, s53
	v_lshlrev_b64 v[250:251], 10, v[22:23]
	v_lshl_add_u64 v[250:251], v[250:251], 0, s[100:101]
	v_lshl_add_u64 v[250:251], v[250:251], 0, v[166:167]
	s_mov_b64 s[26:27], -1
	s_and_b64 vcc, exec, s[38:39]
	s_waitcnt vmcnt(0)
	s_waitcnt lgkmcnt(0)
	v_pk_fma_f32 v[26:27], v[154:155], s[24:25], v[2:3] op_sel_hi:[1,0,1]
	v_pk_fma_f32 v[18:19], v[160:161], s[24:25], v[12:13] op_sel_hi:[1,0,1]
	v_pk_fma_f32 v[20:21], v[158:159], s[24:25], v[10:11] op_sel_hi:[1,0,1]
	v_min_f32_e32 v18, 0x40e00000, v18
	v_min_f32_e32 v20, 0x40e00000, v20
	v_min_f32_e32 v21, 0x40e00000, v21
	v_pk_fma_f32 v[30:31], v[150:151], s[24:25], v[6:7] op_sel_hi:[1,0,1]
	v_min_f32_e32 v19, 0x40e00000, v19
	v_med3_f32 v30, v30, s19, v227
	v_med3_f32 v31, v31, s19, v227
	v_pk_add_f32 v[30:31], v[30:31], 1.0 op_sel_hi:[1,0]
	v_pk_fma_f32 v[32:33], v[148:149], s[24:25], v[16:17] op_sel_hi:[1,0,1]
	v_pk_mul_f32 v[148:149], v[20:21], s[28:29] op_sel_hi:[1,0]
	v_pk_mul_f32 v[20:21], v[20:21], v[30:31]
	v_pk_mul_f32 v[30:31], v[18:19], s[28:29] op_sel_hi:[1,0]
	v_pk_fma_f32 v[24:25], v[152:153], s[24:25], v[8:9] op_sel_hi:[1,0,1]
	v_exp_f32_e32 v30, v30
	v_exp_f32_e32 v31, v31
	v_med3_f32 v24, v24, s19, v227
	v_med3_f32 v25, v25, s19, v227
	v_pk_add_f32 v[24:25], v[24:25], 1.0 op_sel_hi:[1,0]
	v_pk_add_f32 v[30:31], v[30:31], 1.0 op_sel_hi:[1,0]
	v_pk_mul_f32 v[18:19], v[18:19], v[24:25]
	v_rcp_f32_e32 v30, v30
	v_rcp_f32_e32 v31, v31
	v_pk_fma_f32 v[146:147], v[146:147], s[24:25], v[14:15] op_sel_hi:[1,0,1]
	v_pk_fma_f32 v[28:29], v[156:157], s[24:25], v[4:5] op_sel_hi:[1,0,1]
	v_exp_f32_e32 v148, v148
	v_pk_mul_f32 v[24:25], v[18:19], v[30:31]
	v_min_f32_e32 v18, 0x40e00000, v26
	v_min_f32_e32 v19, 0x40e00000, v27
	v_pk_mul_f32 v[30:31], v[18:19], s[28:29] op_sel_hi:[1,0]
	v_med3_f32 v26, v146, s19, v227
	v_exp_f32_e32 v30, v30
	v_exp_f32_e32 v31, v31
	v_med3_f32 v27, v147, s19, v227
	v_pk_add_f32 v[26:27], v[26:27], 1.0 op_sel_hi:[1,0]
	v_exp_f32_e32 v149, v149
	v_pk_add_f32 v[30:31], v[30:31], 1.0 op_sel_hi:[1,0]
	v_pk_mul_f32 v[18:19], v[18:19], v[26:27]
	v_rcp_f32_e32 v30, v30
	v_rcp_f32_e32 v31, v31
	v_pk_add_f32 v[148:149], v[148:149], 1.0 op_sel_hi:[1,0]
	v_pk_fma_f32 v[134:135], v[134:135], s[24:25], v[6:7] op_sel_hi:[1,0,1]
	v_rcp_f32_e32 v148, v148
	v_pk_mul_f32 v[26:27], v[18:19], v[30:31]
	v_min_f32_e32 v18, 0x40e00000, v28
	v_min_f32_e32 v19, 0x40e00000, v29
	v_pk_mul_f32 v[30:31], v[18:19], s[28:29] op_sel_hi:[1,0]
	v_rcp_f32_e32 v149, v149
	v_exp_f32_e32 v30, v30
	v_exp_f32_e32 v31, v31
	v_med3_f32 v28, v32, s19, v227
	v_med3_f32 v29, v33, s19, v227
	v_pk_add_f32 v[28:29], v[28:29], 1.0 op_sel_hi:[1,0]
	v_pk_add_f32 v[30:31], v[30:31], 1.0 op_sel_hi:[1,0]
	v_pk_mul_f32 v[18:19], v[18:19], v[28:29]
	v_rcp_f32_e32 v30, v30
	v_rcp_f32_e32 v31, v31
	v_pk_mul_f32 v[20:21], v[20:21], v[148:149]
	v_pk_fma_f32 v[32:33], v[136:137], s[24:25], v[8:9] op_sel_hi:[1,0,1]
	v_pk_fma_f32 v[142:143], v[142:143], s[24:25], v[10:11] op_sel_hi:[1,0,1]
	v_pk_mul_f32 v[28:29], v[18:19], v[30:31]
	v_cvt_pk_fp8_f32 v19, v26, v27
	v_cvt_pk_fp8_f32 v18, v20, v21
	v_pk_fma_f32 v[30:31], v[144:145], s[24:25], v[12:13] op_sel_hi:[1,0,1]
	v_pk_fma_f32 v[20:21], v[140:141], s[24:25], v[4:5] op_sel_hi:[1,0,1]
	v_cvt_pk_fp8_f32 v19, v28, v29 op_sel:[0,0,1]
	v_pk_fma_f32 v[28:29], v[130:131], s[24:25], v[14:15] op_sel_hi:[1,0,1]
	v_cvt_pk_fp8_f32 v18, v24, v25 op_sel:[0,0,1]
	v_pk_fma_f32 v[26:27], v[138:139], s[24:25], v[2:3] op_sel_hi:[1,0,1]
	v_pk_fma_f32 v[24:25], v[132:133], s[24:25], v[16:17] op_sel_hi:[1,0,1]
	v_med3_f32 v132, v134, s19, v227
	v_med3_f32 v133, v135, s19, v227
	v_med3_f32 v32, v32, s19, v227
	v_med3_f32 v33, v33, s19, v227
	v_med3_f32 v28, v28, s19, v227
	v_med3_f32 v29, v29, s19, v227
	v_min_f32_e32 v130, 0x40e00000, v142
	v_min_f32_e32 v131, 0x40e00000, v143
	v_pk_add_f32 v[132:133], v[132:133], 1.0 op_sel_hi:[1,0]
	v_min_f32_e32 v30, 0x40e00000, v30
	v_min_f32_e32 v31, 0x40e00000, v31
	v_pk_add_f32 v[32:33], v[32:33], 1.0 op_sel_hi:[1,0]
	v_min_f32_e32 v26, 0x40e00000, v26
	v_min_f32_e32 v27, 0x40e00000, v27
	v_pk_add_f32 v[28:29], v[28:29], 1.0 op_sel_hi:[1,0]
	v_min_f32_e32 v20, 0x40e00000, v20
	v_min_f32_e32 v21, 0x40e00000, v21
	v_pk_mul_f32 v[134:135], v[130:131], s[28:29] op_sel_hi:[1,0]
	v_pk_mul_f32 v[130:131], v[130:131], v[132:133]
	v_pk_mul_f32 v[132:133], v[30:31], s[28:29] op_sel_hi:[1,0]
	v_pk_mul_f32 v[30:31], v[30:31], v[32:33]
	v_pk_mul_f32 v[32:33], v[26:27], s[28:29] op_sel_hi:[1,0]
	v_pk_mul_f32 v[26:27], v[26:27], v[28:29]
	v_pk_mul_f32 v[28:29], v[20:21], s[28:29] op_sel_hi:[1,0]
	v_exp_f32_e32 v134, v134
	v_exp_f32_e32 v135, v135
	v_exp_f32_e32 v32, v32
	v_exp_f32_e32 v33, v33
	v_exp_f32_e32 v28, v28
	v_exp_f32_e32 v29, v29
	v_pk_add_f32 v[134:135], v[134:135], 1.0 op_sel_hi:[1,0]
	v_exp_f32_e32 v132, v132
	v_exp_f32_e32 v133, v133
	v_pk_add_f32 v[32:33], v[32:33], 1.0 op_sel_hi:[1,0]
	v_pk_add_f32 v[28:29], v[28:29], 1.0 op_sel_hi:[1,0]
	v_rcp_f32_e32 v134, v134
	v_rcp_f32_e32 v135, v135
	v_rcp_f32_e32 v32, v32
	v_rcp_f32_e32 v33, v33
	v_rcp_f32_e32 v28, v28
	v_rcp_f32_e32 v29, v29
	v_med3_f32 v24, v24, s19, v227
	v_med3_f32 v25, v25, s19, v227
	v_pk_add_f32 v[24:25], v[24:25], 1.0 op_sel_hi:[1,0]
	v_pk_add_f32 v[132:133], v[132:133], 1.0 op_sel_hi:[1,0]
	v_pk_mul_f32 v[20:21], v[20:21], v[24:25]
	v_pk_mul_f32 v[130:131], v[130:131], v[134:135]
	v_rcp_f32_e32 v132, v132
	v_rcp_f32_e32 v133, v133
	v_pk_mul_f32 v[26:27], v[26:27], v[32:33]
	v_pk_mul_f32 v[24:25], v[20:21], v[28:29]
	v_cvt_pk_fp8_f32 v20, v130, v131
	v_cvt_pk_fp8_f32 v21, v26, v27
	v_pk_mul_f32 v[30:31], v[30:31], v[132:133]
	v_pk_fma_f32 v[32:33], v[116:117], s[24:25], v[16:17] op_sel_hi:[1,0,1]
	v_cvt_pk_fp8_f32 v20, v30, v31 op_sel:[0,0,1]
	v_cvt_pk_fp8_f32 v21, v24, v25 op_sel:[0,0,1]
	v_permlane16_swap_b32_e32 v18, v20
	v_permlane16_swap_b32_e32 v19, v21
	v_pk_fma_f32 v[30:31], v[118:119], s[24:25], v[6:7] op_sel_hi:[1,0,1]
	global_store_dwordx4 v[250:251], v[18:21], off
	v_med3_f32 v30, v30, s19, v227
	v_med3_f32 v31, v31, s19, v227
	v_pk_fma_f32 v[18:19], v[128:129], s[24:25], v[12:13] op_sel_hi:[1,0,1]
	v_pk_fma_f32 v[20:21], v[126:127], s[24:25], v[10:11] op_sel_hi:[1,0,1]
	v_pk_add_f32 v[30:31], v[30:31], 1.0 op_sel_hi:[1,0]
	v_min_f32_e32 v20, 0x40e00000, v20
	v_min_f32_e32 v21, 0x40e00000, v21
	v_min_f32_e32 v18, 0x40e00000, v18
	v_min_f32_e32 v19, 0x40e00000, v19
	v_pk_mul_f32 v[116:117], v[20:21], s[28:29] op_sel_hi:[1,0]
	v_pk_mul_f32 v[20:21], v[20:21], v[30:31]
	v_pk_mul_f32 v[30:31], v[18:19], s[28:29] op_sel_hi:[1,0]
	v_pk_fma_f32 v[28:29], v[120:121], s[24:25], v[8:9] op_sel_hi:[1,0,1]
	v_exp_f32_e32 v30, v30
	v_exp_f32_e32 v31, v31
	v_med3_f32 v28, v28, s19, v227
	v_med3_f32 v29, v29, s19, v227
	v_pk_add_f32 v[28:29], v[28:29], 1.0 op_sel_hi:[1,0]
	v_pk_add_f32 v[30:31], v[30:31], 1.0 op_sel_hi:[1,0]
	v_pk_fma_f32 v[26:27], v[122:123], s[24:25], v[2:3] op_sel_hi:[1,0,1]
	v_rcp_f32_e32 v30, v30
	v_rcp_f32_e32 v31, v31
	v_pk_mul_f32 v[18:19], v[18:19], v[28:29]
	v_pk_fma_f32 v[114:115], v[114:115], s[24:25], v[14:15] op_sel_hi:[1,0,1]
	v_pk_fma_f32 v[24:25], v[124:125], s[24:25], v[4:5] op_sel_hi:[1,0,1]
	v_pk_mul_f32 v[28:29], v[18:19], v[30:31]
	v_min_f32_e32 v18, 0x40e00000, v26
	v_min_f32_e32 v19, 0x40e00000, v27
	v_pk_mul_f32 v[30:31], v[18:19], s[28:29] op_sel_hi:[1,0]
	v_med3_f32 v26, v114, s19, v227
	v_exp_f32_e32 v30, v30
	v_exp_f32_e32 v31, v31
	v_med3_f32 v27, v115, s19, v227
	v_pk_add_f32 v[26:27], v[26:27], 1.0 op_sel_hi:[1,0]
	v_exp_f32_e32 v116, v116
	v_pk_add_f32 v[30:31], v[30:31], 1.0 op_sel_hi:[1,0]
	v_pk_mul_f32 v[18:19], v[18:19], v[26:27]
	v_rcp_f32_e32 v30, v30
	v_rcp_f32_e32 v31, v31
	v_exp_f32_e32 v117, v117
	v_pk_fma_f32 v[98:99], v[98:99], s[24:25], v[14:15] op_sel_hi:[1,0,1]
	v_pk_fma_f32 v[100:101], v[100:101], s[24:25], v[16:17] op_sel_hi:[1,0,1]
	v_pk_mul_f32 v[26:27], v[18:19], v[30:31]
	v_min_f32_e32 v18, 0x40e00000, v24
	v_min_f32_e32 v19, 0x40e00000, v25
	v_pk_mul_f32 v[30:31], v[18:19], s[28:29] op_sel_hi:[1,0]
	v_med3_f32 v24, v32, s19, v227
	v_exp_f32_e32 v30, v30
	v_exp_f32_e32 v31, v31
	v_med3_f32 v25, v33, s19, v227
	v_pk_add_f32 v[24:25], v[24:25], 1.0 op_sel_hi:[1,0]
	v_pk_add_f32 v[116:117], v[116:117], 1.0 op_sel_hi:[1,0]
	v_pk_add_f32 v[30:31], v[30:31], 1.0 op_sel_hi:[1,0]
	v_pk_mul_f32 v[18:19], v[18:19], v[24:25]
	v_rcp_f32_e32 v30, v30
	v_rcp_f32_e32 v31, v31
	v_rcp_f32_e32 v116, v116
	v_rcp_f32_e32 v117, v117
	v_pk_fma_f32 v[32:33], v[102:103], s[24:25], v[6:7] op_sel_hi:[1,0,1]
	v_pk_mul_f32 v[24:25], v[18:19], v[30:31]
	v_cvt_pk_fp8_f32 v19, v26, v27
	v_pk_mul_f32 v[20:21], v[20:21], v[116:117]
	v_cvt_pk_fp8_f32 v18, v20, v21
	v_cvt_pk_fp8_f32 v19, v24, v25 op_sel:[0,0,1]
	v_pk_fma_f32 v[20:21], v[112:113], s[24:25], v[12:13] op_sel_hi:[1,0,1]
	v_pk_fma_f32 v[24:25], v[110:111], s[24:25], v[10:11] op_sel_hi:[1,0,1]
	v_med3_f32 v32, v32, s19, v227
	v_med3_f32 v33, v33, s19, v227
	v_min_f32_e32 v24, 0x40e00000, v24
	v_min_f32_e32 v25, 0x40e00000, v25
	v_pk_add_f32 v[32:33], v[32:33], 1.0 op_sel_hi:[1,0]
	v_min_f32_e32 v20, 0x40e00000, v20
	v_min_f32_e32 v21, 0x40e00000, v21
	v_pk_mul_f32 v[102:103], v[24:25], s[28:29] op_sel_hi:[1,0]
	v_pk_mul_f32 v[24:25], v[24:25], v[32:33]
	v_pk_mul_f32 v[32:33], v[20:21], s[28:29] op_sel_hi:[1,0]
	v_pk_fma_f32 v[30:31], v[104:105], s[24:25], v[8:9] op_sel_hi:[1,0,1]
	v_exp_f32_e32 v32, v32
	v_exp_f32_e32 v33, v33
	v_med3_f32 v30, v30, s19, v227
	v_med3_f32 v31, v31, s19, v227
	v_pk_add_f32 v[30:31], v[30:31], 1.0 op_sel_hi:[1,0]
	v_pk_add_f32 v[32:33], v[32:33], 1.0 op_sel_hi:[1,0]
	v_cvt_pk_fp8_f32 v18, v28, v29 op_sel:[0,0,1]
	v_rcp_f32_e32 v32, v32
	v_rcp_f32_e32 v33, v33
	v_pk_fma_f32 v[28:29], v[106:107], s[24:25], v[2:3] op_sel_hi:[1,0,1]
	v_pk_mul_f32 v[20:21], v[20:21], v[30:31]
	v_pk_fma_f32 v[26:27], v[108:109], s[24:25], v[4:5] op_sel_hi:[1,0,1]
	v_pk_mul_f32 v[30:31], v[20:21], v[32:33]
	v_min_f32_e32 v20, 0x40e00000, v28
	v_min_f32_e32 v21, 0x40e00000, v29
	v_pk_mul_f32 v[32:33], v[20:21], s[28:29] op_sel_hi:[1,0]
	v_med3_f32 v28, v98, s19, v227
	v_exp_f32_e32 v32, v32
	v_exp_f32_e32 v33, v33
	v_med3_f32 v29, v99, s19, v227
	v_pk_add_f32 v[28:29], v[28:29], 1.0 op_sel_hi:[1,0]
	v_exp_f32_e32 v102, v102
	v_pk_add_f32 v[32:33], v[32:33], 1.0 op_sel_hi:[1,0]
	v_pk_mul_f32 v[20:21], v[20:21], v[28:29]
	v_rcp_f32_e32 v32, v32
	v_rcp_f32_e32 v33, v33
	v_exp_f32_e32 v103, v103
	v_pk_fma_f32 v[82:83], v[82:83], s[24:25], v[14:15] op_sel_hi:[1,0,1]
	v_pk_fma_f32 v[84:85], v[84:85], s[24:25], v[16:17] op_sel_hi:[1,0,1]
	v_pk_mul_f32 v[28:29], v[20:21], v[32:33]
	v_min_f32_e32 v20, 0x40e00000, v26
	v_min_f32_e32 v21, 0x40e00000, v27
	v_pk_mul_f32 v[32:33], v[20:21], s[28:29] op_sel_hi:[1,0]
	v_pk_add_f32 v[102:103], v[102:103], 1.0 op_sel_hi:[1,0]
	v_exp_f32_e32 v32, v32
	v_exp_f32_e32 v33, v33
	v_rcp_f32_e32 v102, v102
	v_rcp_f32_e32 v103, v103
	v_med3_f32 v26, v100, s19, v227
	v_pk_add_f32 v[32:33], v[32:33], 1.0 op_sel_hi:[1,0]
	v_med3_f32 v27, v101, s19, v227
	v_rcp_f32_e32 v32, v32
	v_rcp_f32_e32 v33, v33
	v_pk_add_f32 v[26:27], v[26:27], 1.0 op_sel_hi:[1,0]
	v_pk_mul_f32 v[24:25], v[24:25], v[102:103]
	v_pk_mul_f32 v[20:21], v[20:21], v[26:27]
	s_nop 0
	v_pk_mul_f32 v[26:27], v[20:21], v[32:33]
	v_cvt_pk_fp8_f32 v20, v24, v25
	v_cvt_pk_fp8_f32 v21, v28, v29
	v_cvt_pk_fp8_f32 v20, v30, v31 op_sel:[0,0,1]
	v_cvt_pk_fp8_f32 v21, v26, v27 op_sel:[0,0,1]
	v_permlane16_swap_b32_e32 v18, v20
	v_permlane16_swap_b32_e32 v19, v21
	s_mov_b64 s[100:101], 0x8000
	v_lshl_add_u64 v[24:25], v[250:251], 0, s[100:101]
	v_pk_fma_f32 v[32:33], v[86:87], s[24:25], v[6:7] op_sel_hi:[1,0,1]
	global_store_dwordx4 v[24:25], v[18:21], off
	v_med3_f32 v32, v32, s19, v227
	v_med3_f32 v33, v33, s19, v227
	v_pk_fma_f32 v[18:19], v[96:97], s[24:25], v[12:13] op_sel_hi:[1,0,1]
	v_pk_fma_f32 v[20:21], v[94:95], s[24:25], v[10:11] op_sel_hi:[1,0,1]
	v_pk_add_f32 v[32:33], v[32:33], 1.0 op_sel_hi:[1,0]
	v_min_f32_e32 v20, 0x40e00000, v20
	v_min_f32_e32 v21, 0x40e00000, v21
	v_min_f32_e32 v18, 0x40e00000, v18
	v_min_f32_e32 v19, 0x40e00000, v19
	v_pk_mul_f32 v[86:87], v[20:21], s[28:29] op_sel_hi:[1,0]
	v_pk_mul_f32 v[20:21], v[20:21], v[32:33]
	v_pk_mul_f32 v[32:33], v[18:19], s[28:29] op_sel_hi:[1,0]
	v_pk_fma_f32 v[30:31], v[88:89], s[24:25], v[8:9] op_sel_hi:[1,0,1]
	v_exp_f32_e32 v32, v32
	v_exp_f32_e32 v33, v33
	v_med3_f32 v30, v30, s19, v227
	v_med3_f32 v31, v31, s19, v227
	v_pk_add_f32 v[30:31], v[30:31], 1.0 op_sel_hi:[1,0]
	v_pk_add_f32 v[32:33], v[32:33], 1.0 op_sel_hi:[1,0]
	v_pk_fma_f32 v[28:29], v[90:91], s[24:25], v[2:3] op_sel_hi:[1,0,1]
	v_rcp_f32_e32 v32, v32
	v_rcp_f32_e32 v33, v33
	v_pk_mul_f32 v[18:19], v[18:19], v[30:31]
	v_pk_fma_f32 v[26:27], v[92:93], s[24:25], v[4:5] op_sel_hi:[1,0,1]
	v_exp_f32_e32 v86, v86
	v_pk_mul_f32 v[30:31], v[18:19], v[32:33]
	v_min_f32_e32 v18, 0x40e00000, v28
	v_min_f32_e32 v19, 0x40e00000, v29
	v_pk_mul_f32 v[32:33], v[18:19], s[28:29] op_sel_hi:[1,0]
	v_med3_f32 v28, v82, s19, v227
	v_exp_f32_e32 v32, v32
	v_exp_f32_e32 v33, v33
	v_med3_f32 v29, v83, s19, v227
	v_pk_add_f32 v[28:29], v[28:29], 1.0 op_sel_hi:[1,0]
	v_exp_f32_e32 v87, v87
	v_pk_add_f32 v[32:33], v[32:33], 1.0 op_sel_hi:[1,0]
	v_pk_mul_f32 v[18:19], v[18:19], v[28:29]
	v_rcp_f32_e32 v32, v32
	v_rcp_f32_e32 v33, v33
	v_pk_add_f32 v[86:87], v[86:87], 1.0 op_sel_hi:[1,0]
	v_rcp_f32_e32 v86, v86
	v_pk_mul_f32 v[28:29], v[18:19], v[32:33]
	v_min_f32_e32 v18, 0x40e00000, v26
	v_min_f32_e32 v19, 0x40e00000, v27
	v_pk_mul_f32 v[32:33], v[18:19], s[28:29] op_sel_hi:[1,0]
	v_rcp_f32_e32 v87, v87
	v_exp_f32_e32 v32, v32
	v_exp_f32_e32 v33, v33
	v_med3_f32 v26, v84, s19, v227
	v_med3_f32 v27, v85, s19, v227
	v_pk_add_f32 v[26:27], v[26:27], 1.0 op_sel_hi:[1,0]
	v_pk_add_f32 v[32:33], v[32:33], 1.0 op_sel_hi:[1,0]
	v_pk_mul_f32 v[18:19], v[18:19], v[26:27]
	v_rcp_f32_e32 v32, v32
	v_rcp_f32_e32 v33, v33
	v_pk_mul_f32 v[20:21], v[20:21], v[86:87]
	v_pk_mul_f32 v[26:27], v[18:19], v[32:33]
	v_cvt_pk_fp8_f32 v18, v20, v21
	v_cvt_pk_fp8_f32 v19, v28, v29
	v_pk_fma_f32 v[20:21], v[72:73], s[24:25], v[12:13] op_sel_hi:[1,0,1]
	v_cvt_pk_fp8_f32 v18, v30, v31 op_sel:[0,0,1]
	v_pk_fma_f32 v[30:31], v[66:67], s[24:25], v[2:3] op_sel_hi:[1,0,1]
	v_pk_fma_f32 v[66:67], v[78:79], s[24:25], v[6:7] op_sel_hi:[1,0,1]
	v_cvt_pk_fp8_f32 v19, v26, v27 op_sel:[0,0,1]
	v_pk_fma_f32 v[26:27], v[70:71], s[24:25], v[10:11] op_sel_hi:[1,0,1]
	v_med3_f32 v66, v66, s19, v227
	v_med3_f32 v67, v67, s19, v227
	v_min_f32_e32 v26, 0x40e00000, v26
	v_min_f32_e32 v27, 0x40e00000, v27
	v_pk_add_f32 v[66:67], v[66:67], 1.0 op_sel_hi:[1,0]
	v_min_f32_e32 v20, 0x40e00000, v20
	v_min_f32_e32 v21, 0x40e00000, v21
	v_pk_mul_f32 v[72:73], v[26:27], s[28:29] op_sel_hi:[1,0]
	v_pk_mul_f32 v[26:27], v[26:27], v[66:67]
	v_pk_mul_f32 v[66:67], v[20:21], s[28:29] op_sel_hi:[1,0]
	v_pk_fma_f32 v[32:33], v[80:81], s[24:25], v[8:9] op_sel_hi:[1,0,1]
	v_exp_f32_e32 v66, v66
	v_exp_f32_e32 v67, v67
	v_med3_f32 v32, v32, s19, v227
	v_med3_f32 v33, v33, s19, v227
	v_pk_add_f32 v[32:33], v[32:33], 1.0 op_sel_hi:[1,0]
	v_pk_add_f32 v[66:67], v[66:67], 1.0 op_sel_hi:[1,0]
	v_pk_mul_f32 v[20:21], v[20:21], v[32:33]
	v_rcp_f32_e32 v66, v66
	v_rcp_f32_e32 v67, v67
	v_pk_fma_f32 v[70:71], v[74:75], s[24:25], v[14:15] op_sel_hi:[1,0,1]
	v_pk_fma_f32 v[28:29], v[68:69], s[24:25], v[4:5] op_sel_hi:[1,0,1]
	v_exp_f32_e32 v72, v72
	v_pk_mul_f32 v[32:33], v[20:21], v[66:67]
	v_min_f32_e32 v20, 0x40e00000, v30
	v_min_f32_e32 v21, 0x40e00000, v31
	v_pk_mul_f32 v[66:67], v[20:21], s[28:29] op_sel_hi:[1,0]
	v_med3_f32 v30, v70, s19, v227
	v_exp_f32_e32 v66, v66
	v_exp_f32_e32 v67, v67
	v_med3_f32 v31, v71, s19, v227
	v_pk_add_f32 v[30:31], v[30:31], 1.0 op_sel_hi:[1,0]
	v_exp_f32_e32 v73, v73
	v_pk_add_f32 v[66:67], v[66:67], 1.0 op_sel_hi:[1,0]
	v_pk_mul_f32 v[20:21], v[20:21], v[30:31]
	v_rcp_f32_e32 v66, v66
	v_rcp_f32_e32 v67, v67
	v_pk_add_f32 v[72:73], v[72:73], 1.0 op_sel_hi:[1,0]
	v_pk_fma_f32 v[68:69], v[76:77], s[24:25], v[16:17] op_sel_hi:[1,0,1]
	v_rcp_f32_e32 v72, v72
	v_pk_mul_f32 v[30:31], v[20:21], v[66:67]
	v_min_f32_e32 v20, 0x40e00000, v28
	v_min_f32_e32 v21, 0x40e00000, v29
	v_pk_mul_f32 v[66:67], v[20:21], s[28:29] op_sel_hi:[1,0]
	v_rcp_f32_e32 v73, v73
	v_exp_f32_e32 v66, v66
	v_exp_f32_e32 v67, v67
	v_med3_f32 v28, v68, s19, v227
	v_med3_f32 v29, v69, s19, v227
	v_pk_add_f32 v[28:29], v[28:29], 1.0 op_sel_hi:[1,0]
	v_pk_add_f32 v[66:67], v[66:67], 1.0 op_sel_hi:[1,0]
	v_pk_mul_f32 v[20:21], v[20:21], v[28:29]
	v_rcp_f32_e32 v66, v66
	v_rcp_f32_e32 v67, v67
	v_pk_mul_f32 v[26:27], v[26:27], v[72:73]
	v_pk_mul_f32 v[28:29], v[20:21], v[66:67]
	v_cvt_pk_fp8_f32 v20, v26, v27
	v_cvt_pk_fp8_f32 v21, v30, v31
	s_mov_b64 s[100:101], 0x20000
	v_lshl_add_u64 v[24:25], v[250:251], 0, s[100:101]
	v_cvt_pk_fp8_f32 v20, v32, v33 op_sel:[0,0,1]
	v_cvt_pk_fp8_f32 v21, v28, v29 op_sel:[0,0,1]
	v_pk_fma_f32 v[30:31], v[62:63], s[24:25], v[6:7] op_sel_hi:[1,0,1]
	v_pk_fma_f32 v[28:29], v[64:65], s[24:25], v[8:9] op_sel_hi:[1,0,1]
	v_permlane16_swap_b32_e32 v18, v20
	v_permlane16_swap_b32_e32 v19, v21
	global_store_dwordx4 v[24:25], v[18:21], off
	v_med3_f32 v30, v30, s19, v227
	v_med3_f32 v31, v31, s19, v227
	v_pk_fma_f32 v[18:19], v[56:57], s[24:25], v[12:13] op_sel_hi:[1,0,1]
	v_pk_fma_f32 v[20:21], v[54:55], s[24:25], v[10:11] op_sel_hi:[1,0,1]
	v_pk_add_f32 v[30:31], v[30:31], 1.0 op_sel_hi:[1,0]
	v_min_f32_e32 v20, 0x40e00000, v20
	v_min_f32_e32 v21, 0x40e00000, v21
	v_min_f32_e32 v18, 0x40e00000, v18
	v_min_f32_e32 v19, 0x40e00000, v19
	v_pk_fma_f32 v[24:25], v[52:53], s[24:25], v[4:5] op_sel_hi:[1,0,1]
	v_pk_mul_f32 v[52:53], v[20:21], s[28:29] op_sel_hi:[1,0]
	v_pk_mul_f32 v[20:21], v[20:21], v[30:31]
	v_pk_mul_f32 v[30:31], v[18:19], s[28:29] op_sel_hi:[1,0]
	v_med3_f32 v28, v28, s19, v227
	v_exp_f32_e32 v30, v30
	v_exp_f32_e32 v31, v31
	v_med3_f32 v29, v29, s19, v227
	v_pk_add_f32 v[28:29], v[28:29], 1.0 op_sel_hi:[1,0]
	v_pk_fma_f32 v[26:27], v[50:51], s[24:25], v[2:3] op_sel_hi:[1,0,1]
	v_pk_add_f32 v[30:31], v[30:31], 1.0 op_sel_hi:[1,0]
	v_pk_mul_f32 v[18:19], v[18:19], v[28:29]
	v_rcp_f32_e32 v30, v30
	v_rcp_f32_e32 v31, v31
	v_pk_fma_f32 v[50:51], v[58:59], s[24:25], v[14:15] op_sel_hi:[1,0,1]
	v_exp_f32_e32 v52, v52
	v_exp_f32_e32 v53, v53
	v_pk_mul_f32 v[28:29], v[18:19], v[30:31]
	v_min_f32_e32 v18, 0x40e00000, v26
	v_min_f32_e32 v19, 0x40e00000, v27
	v_pk_mul_f32 v[30:31], v[18:19], s[28:29] op_sel_hi:[1,0]
	v_med3_f32 v26, v50, s19, v227
	v_exp_f32_e32 v30, v30
	v_exp_f32_e32 v31, v31
	v_med3_f32 v27, v51, s19, v227
	v_pk_add_f32 v[26:27], v[26:27], 1.0 op_sel_hi:[1,0]
	v_pk_add_f32 v[52:53], v[52:53], 1.0 op_sel_hi:[1,0]
	v_pk_add_f32 v[30:31], v[30:31], 1.0 op_sel_hi:[1,0]
	v_pk_mul_f32 v[18:19], v[18:19], v[26:27]
	v_rcp_f32_e32 v30, v30
	v_rcp_f32_e32 v31, v31
	v_pk_fma_f32 v[32:33], v[60:61], s[24:25], v[16:17] op_sel_hi:[1,0,1]
	v_rcp_f32_e32 v52, v52
	v_rcp_f32_e32 v53, v53
	v_pk_mul_f32 v[26:27], v[18:19], v[30:31]
	v_min_f32_e32 v18, 0x40e00000, v24
	v_min_f32_e32 v19, 0x40e00000, v25
	v_pk_mul_f32 v[30:31], v[18:19], s[28:29] op_sel_hi:[1,0]
	v_med3_f32 v24, v32, s19, v227
	v_exp_f32_e32 v30, v30
	v_exp_f32_e32 v31, v31
	v_med3_f32 v25, v33, s19, v227
	v_pk_add_f32 v[24:25], v[24:25], 1.0 op_sel_hi:[1,0]
	v_pk_fma_f32 v[6:7], v[46:47], s[24:25], v[6:7] op_sel_hi:[1,0,1]
	v_pk_add_f32 v[30:31], v[30:31], 1.0 op_sel_hi:[1,0]
	v_pk_mul_f32 v[18:19], v[18:19], v[24:25]
	v_rcp_f32_e32 v30, v30
	v_rcp_f32_e32 v31, v31
	v_pk_fma_f32 v[10:11], v[38:39], s[24:25], v[10:11] op_sel_hi:[1,0,1]
	v_med3_f32 v6, v6, s19, v227
	v_med3_f32 v7, v7, s19, v227
	v_pk_mul_f32 v[20:21], v[20:21], v[52:53]
	v_pk_mul_f32 v[24:25], v[18:19], v[30:31]
	v_pk_fma_f32 v[12:13], v[40:41], s[24:25], v[12:13] op_sel_hi:[1,0,1]
	v_min_f32_e32 v10, 0x40e00000, v10
	v_min_f32_e32 v11, 0x40e00000, v11
	v_pk_add_f32 v[6:7], v[6:7], 1.0 op_sel_hi:[1,0]
	v_cvt_pk_fp8_f32 v18, v20, v21
	v_pk_mul_f32 v[20:21], v[10:11], s[28:29] op_sel_hi:[1,0]
	v_pk_mul_f32 v[6:7], v[10:11], v[6:7]
	v_min_f32_e32 v10, 0x40e00000, v12
	v_min_f32_e32 v11, 0x40e00000, v13
	v_pk_mul_f32 v[12:13], v[10:11], s[28:29] op_sel_hi:[1,0]
	v_pk_fma_f32 v[8:9], v[48:49], s[24:25], v[8:9] op_sel_hi:[1,0,1]
	v_exp_f32_e32 v12, v12
	v_exp_f32_e32 v13, v13
	v_med3_f32 v8, v8, s19, v227
	v_med3_f32 v9, v9, s19, v227
	v_pk_fma_f32 v[2:3], v[34:35], s[24:25], v[2:3] op_sel_hi:[1,0,1]
	v_pk_add_f32 v[12:13], v[12:13], 1.0 op_sel_hi:[1,0]
	v_pk_add_f32 v[8:9], v[8:9], 1.0 op_sel_hi:[1,0]
	v_rcp_f32_e32 v12, v12
	v_rcp_f32_e32 v13, v13
	v_pk_mul_f32 v[8:9], v[10:11], v[8:9]
	v_min_f32_e32 v2, 0x40e00000, v2
	v_min_f32_e32 v3, 0x40e00000, v3
	v_pk_mul_f32 v[8:9], v[8:9], v[12:13]
	v_pk_mul_f32 v[12:13], v[2:3], s[28:29] op_sel_hi:[1,0]
	v_pk_fma_f32 v[14:15], v[42:43], s[24:25], v[14:15] op_sel_hi:[1,0,1]
	v_exp_f32_e32 v12, v12
	v_exp_f32_e32 v13, v13
	v_exp_f32_e32 v20, v20
	v_exp_f32_e32 v21, v21
	v_med3_f32 v10, v14, s19, v227
	v_pk_add_f32 v[12:13], v[12:13], 1.0 op_sel_hi:[1,0]
	v_med3_f32 v11, v15, s19, v227
	v_rcp_f32_e32 v12, v12
	v_rcp_f32_e32 v13, v13
	v_pk_fma_f32 v[4:5], v[36:37], s[24:25], v[4:5] op_sel_hi:[1,0,1]
	v_pk_add_f32 v[10:11], v[10:11], 1.0 op_sel_hi:[1,0]
	v_min_f32_e32 v4, 0x40e00000, v4
	v_pk_mul_f32 v[2:3], v[2:3], v[10:11]
	v_min_f32_e32 v5, 0x40e00000, v5
	v_pk_mul_f32 v[2:3], v[2:3], v[12:13]
	v_pk_mul_f32 v[12:13], v[4:5], s[28:29] op_sel_hi:[1,0]
	v_pk_add_f32 v[20:21], v[20:21], 1.0 op_sel_hi:[1,0]
	v_exp_f32_e32 v12, v12
	v_exp_f32_e32 v13, v13
	v_rcp_f32_e32 v20, v20
	v_rcp_f32_e32 v21, v21
	v_pk_add_f32 v[12:13], v[12:13], 1.0 op_sel_hi:[1,0]
	v_pk_fma_f32 v[16:17], v[44:45], s[24:25], v[16:17] op_sel_hi:[1,0,1]
	v_pk_mul_f32 v[6:7], v[6:7], v[20:21]
	v_rcp_f32_e32 v12, v12
	v_rcp_f32_e32 v13, v13
	v_cvt_pk_fp8_f32 v19, v26, v27
	v_med3_f32 v10, v16, s19, v227
	v_med3_f32 v11, v17, s19, v227
	v_cvt_pk_fp8_f32 v20, v6, v7
	v_cvt_pk_fp8_f32 v21, v2, v3
	v_pk_add_f32 v[10:11], v[10:11], 1.0 op_sel_hi:[1,0]
	v_pk_mul_f32 v[4:5], v[4:5], v[10:11]
	v_pk_mul_f32 v[4:5], v[4:5], v[12:13]
	v_cvt_pk_fp8_f32 v18, v28, v29 op_sel:[0,0,1]
	v_cvt_pk_fp8_f32 v19, v24, v25 op_sel:[0,0,1]
	v_cvt_pk_fp8_f32 v20, v8, v9 op_sel:[0,0,1]
	v_cvt_pk_fp8_f32 v21, v4, v5 op_sel:[0,0,1]
	v_permlane16_swap_b32_e32 v18, v20
	v_permlane16_swap_b32_e32 v19, v21
	s_mov_b64 s[100:101], 0x28000
	v_lshl_add_u64 v[2:3], v[250:251], 0, s[100:101]
	global_store_dwordx4 v[2:3], v[18:21], off
	s_cbranch_vccnz .LBB0_237
	s_andn2_b64 vcc, exec, s[42:43]
	s_cbranch_vccnz .LBB0_236
	s_barrier
	s_branch .LBB0_236
